# baseline (speedup 1.0000x reference)
.LBB1_8:
	s_or_b64 exec, exec, s[4:5]
	v_add_u32_e32 v10, v172, v2
	s_waitcnt vmcnt(1) lgkmcnt(0)
	s_barrier
	v_readfirstlane_b32 s4, v0
	s_cmpk_lt_u32 s4, 0x100
	s_cbranch_scc1 .Lno_stag
	s_nop 15
	s_nop 15
.Lno_stag:
	s_nop 0
	s_nop 0
	s_nop 0
	s_nop 0
	s_nop 0
	s_nop 0
	s_nop 0
	s_nop 0
	s_nop 0
	s_nop 0
	s_nop 0
	ds_read_b128 v[18:21], v10 offset:256
	ds_read_b128 v[22:25], v10 offset:288
	ds_read_b128 v[82:85], v10 offset:320
	ds_read_b128 v[86:89], v10 offset:352
	ds_read_b128 v[74:77], v10 offset:384
	ds_read_b128 v[78:81], v10 offset:416
	ds_read_b128 v[2:5], v213 offset:32768
	ds_read_b128 v[6:9], v213 offset:0
	ds_read_b128 v[66:69], v10 offset:448
	ds_read_b128 v[70:73], v10 offset:480
	ds_read_b128 v[10:13], v213 offset:1024
	s_waitcnt lgkmcnt(3)
	v_pk_mul_f32 v[26:27], v[8:9], v[20:21]
	v_pk_mul_f32 v[28:29], v[6:7], v[18:19]
	ds_read_b128 v[14:17], v213 offset:8192
	s_waitcnt lgkmcnt(1)
	v_pk_mul_f32 v[12:13], v[12:13], v[24:25]
	v_pk_mul_f32 v[10:11], v[10:11], v[22:23]
	v_pk_fma_f32 v[30:31], v[8:9], v[20:21], v[12:13]
	v_pk_fma_f32 v[32:33], v[6:7], v[18:19], v[10:11]
	v_cvt_pk_bf16_f32 v9, v12, v13
	v_cvt_pk_bf16_f32 v7, v26, v27
	v_cvt_pk_bf16_f32 v8, v10, v11
	v_cvt_pk_bf16_f32 v6, v28, v29
	ds_read_b128 v[10:13], v213 offset:33792
	s_nop 0
	v_mfma_f32_32x32x16_bf16 v[34:49], v[2:5], v[6:9], 0
	ds_read_b128 v[6:9], v213 offset:9216
	s_waitcnt lgkmcnt(2)
	v_mul_f32_e32 v26, v16, v20
	v_mul_f32_e32 v27, v17, v21
	v_pk_mul_f32 v[50:51], v[14:15], v[18:19]
	s_mov_b32 s4, 0x3727c5ac
	s_waitcnt lgkmcnt(0)
	v_pk_mul_f32 v[8:9], v[8:9], v[24:25]
	v_pk_mul_f32 v[28:29], v[6:7], v[22:23]
	v_pk_fma_f32 v[90:91], v[16:17], v[20:21], v[8:9]
	v_pk_fma_f32 v[92:93], v[14:15], v[18:19], v[28:29]
	ds_read_b128 v[14:17], v213 offset:2048
	v_cvt_pk_bf16_f32 v9, v8, v9
	v_cvt_pk_bf16_f32 v7, v26, v27
	v_cvt_pk_bf16_f32 v8, v28, v29
	ds_read_b128 v[26:29], v213 offset:3072
	v_cvt_pk_bf16_f32 v6, v50, v51
	s_waitcnt lgkmcnt(1)
	v_pk_mul_f32 v[94:95], v[14:15], v[82:83]
	s_mov_b32 s0, 0x3c800000
	v_mfma_f32_32x32x16_bf16 v[50:65], v[2:5], v[6:9], 0
	v_mul_f32_e32 v2, v16, v84
	v_mul_f32_e32 v3, v17, v85
	s_waitcnt lgkmcnt(0)
	v_mul_f32_e32 v4, v28, v88
	v_mul_f32_e32 v5, v29, v89
	v_pk_mul_f32 v[6:7], v[26:27], v[86:87]
	v_pk_fma_f32 v[8:9], v[16:17], v[84:85], v[4:5]
	v_cvt_pk_bf16_f32 v3, v2, v3
	v_pk_fma_f32 v[14:15], v[14:15], v[82:83], v[6:7]
	v_pk_add_f32 v[26:27], v[8:9], v[30:31]
	v_cvt_pk_bf16_f32 v5, v4, v5
	v_cvt_pk_bf16_f32 v4, v6, v7
	ds_read_b128 v[6:9], v213 offset:10240
	v_pk_add_f32 v[28:29], v[14:15], v[32:33]
	ds_read_b128 v[14:17], v213 offset:11264
	v_cvt_pk_bf16_f32 v2, v94, v95
	s_waitcnt lgkmcnt(1)
	v_pk_mul_f32 v[30:31], v[6:7], v[82:83]
	v_mov_b64_e32 v[152:153], s[4:5]
	v_mfma_f32_32x32x16_bf16 v[34:49], v[10:13], v[2:5], v[34:49]
	v_mul_f32_e32 v2, v8, v84
	v_mul_f32_e32 v3, v9, v85
	s_waitcnt lgkmcnt(0)
	v_mul_f32_e32 v4, v16, v88
	v_mul_f32_e32 v5, v17, v89
	v_pk_mul_f32 v[14:15], v[14:15], v[86:87]
	v_pk_fma_f32 v[8:9], v[8:9], v[84:85], v[4:5]
	v_pk_fma_f32 v[6:7], v[6:7], v[82:83], v[14:15]
	v_cvt_pk_bf16_f32 v5, v4, v5
	v_cvt_pk_bf16_f32 v3, v2, v3
	v_cvt_pk_bf16_f32 v4, v14, v15
	v_pk_add_f32 v[32:33], v[8:9], v[90:91]
	v_pk_add_f32 v[90:91], v[6:7], v[92:93]
	ds_read_b128 v[6:9], v213 offset:34816
	ds_read_b128 v[14:17], v213 offset:4096
	v_cvt_pk_bf16_f32 v2, v30, v31
	s_mov_b32 s13, 0
	s_mov_b64 s[6:7], 0
	v_mfma_f32_32x32x16_bf16 v[50:65], v[10:13], v[2:5], v[50:65]
	ds_read_b128 v[2:5], v213 offset:5120
	ds_read_b128 v[10:13], v213 offset:12288
	s_waitcnt lgkmcnt(2)
	v_pk_mul_f32 v[30:31], v[16:17], v[76:77]
	v_pk_mul_f32 v[92:93], v[14:15], v[74:75]
	s_waitcnt lgkmcnt(1)
	v_pk_mul_f32 v[4:5], v[4:5], v[80:81]
	v_pk_mul_f32 v[94:95], v[2:3], v[78:79]
	v_pk_fma_f32 v[2:3], v[16:17], v[76:77], v[4:5]
	v_cvt_pk_bf16_f32 v5, v4, v5
	v_pk_add_f32 v[96:97], v[2:3], v[26:27]
	v_cvt_pk_bf16_f32 v3, v30, v31
	v_cvt_pk_bf16_f32 v4, v94, v95
	v_cvt_pk_bf16_f32 v2, v92, v93
	v_pk_fma_f32 v[14:15], v[14:15], v[74:75], v[94:95]
	s_waitcnt lgkmcnt(0)
	v_pk_mul_f32 v[30:31], v[10:11], v[74:75]
	v_mfma_f32_32x32x16_bf16 v[34:49], v[6:9], v[2:5], v[34:49]
	ds_read_b128 v[2:5], v213 offset:13312
	v_add_f32_e32 v98, v14, v28
	v_add_f32_e32 v99, v15, v29
	ds_read_b128 v[14:17], v213 offset:35840
	v_pk_mul_f32 v[26:27], v[12:13], v[76:77]
	s_waitcnt lgkmcnt(1)
	v_pk_mul_f32 v[4:5], v[4:5], v[80:81]
	v_pk_mul_f32 v[28:29], v[2:3], v[78:79]
	v_pk_fma_f32 v[2:3], v[12:13], v[76:77], v[4:5]
	v_pk_fma_f32 v[10:11], v[10:11], v[74:75], v[28:29]
	v_pk_add_f32 v[32:33], v[2:3], v[32:33]
	v_pk_add_f32 v[92:93], v[10:11], v[90:91]
	ds_read_b128 v[10:13], v213 offset:6144
	v_cvt_pk_bf16_f32 v5, v4, v5
	v_cvt_pk_bf16_f32 v3, v26, v27
	v_cvt_pk_bf16_f32 v4, v28, v29
	ds_read_b128 v[26:29], v213 offset:7168
	v_cvt_pk_bf16_f32 v2, v30, v31
	s_waitcnt lgkmcnt(1)
	v_pk_mul_f32 v[30:31], v[10:11], v[66:67]
	v_mfma_f32_32x32x16_bf16 v[50:65], v[6:9], v[2:5], v[50:65]
	v_mul_f32_e32 v2, v12, v68
	v_mul_f32_e32 v3, v13, v69
	s_waitcnt lgkmcnt(0)
	v_mul_f32_e32 v4, v28, v72
	v_mul_f32_e32 v5, v29, v73
	v_pk_mul_f32 v[6:7], v[26:27], v[70:71]
	v_pk_fma_f32 v[8:9], v[12:13], v[68:69], v[4:5]
	v_cvt_pk_bf16_f32 v3, v2, v3
	v_pk_fma_f32 v[10:11], v[10:11], v[66:67], v[6:7]
	v_pk_add_f32 v[94:95], v[8:9], v[96:97]
	v_cvt_pk_bf16_f32 v5, v4, v5
	v_cvt_pk_bf16_f32 v4, v6, v7
	ds_read_b128 v[6:9], v213 offset:14336
	v_pk_add_f32 v[96:97], v[10:11], v[98:99]
	ds_read_b128 v[10:13], v213 offset:15360
	v_cvt_pk_bf16_f32 v2, v30, v31
	s_waitcnt lgkmcnt(1)
	v_pk_mul_f32 v[30:31], v[6:7], v[66:67]
	v_mfma_f32_32x32x16_bf16 v[34:49], v[14:17], v[2:5], v[34:49]
	s_waitcnt lgkmcnt(0)
	v_mul_f32_e32 v10, v10, v70
	v_mul_f32_e32 v11, v11, v71
	v_mul_f32_e32 v2, v8, v68
	v_mul_f32_e32 v3, v9, v69
	v_pk_mul_f32 v[4:5], v[12:13], v[72:73]
	v_pk_fma_f32 v[6:7], v[6:7], v[66:67], v[10:11]
	v_pk_fma_f32 v[8:9], v[8:9], v[68:69], v[4:5]
	v_pk_add_f32 v[92:93], v[6:7], v[92:93]
	v_cvt_pk_bf16_f32 v3, v2, v3
	v_pk_add_f32 v[90:91], v[8:9], v[32:33]
	v_cvt_pk_bf16_f32 v5, v4, v5
	v_cvt_pk_bf16_f32 v4, v10, v11
	ds_read_b128 v[26:29], v213 offset:36864
	ds_read_b128 v[6:9], v213 offset:16384
	v_cvt_pk_bf16_f32 v2, v30, v31
	ds_read_b128 v[98:101], v213 offset:25600
	ds_read_b128 v[102:105], v213 offset:37888
	v_mfma_f32_32x32x16_bf16 v[50:65], v[14:17], v[2:5], v[50:65]
	ds_read_b128 v[2:5], v213 offset:17408
	ds_read_b128 v[30:33], v213 offset:24576
	s_waitcnt lgkmcnt(4)
	v_pk_mul_f32 v[12:13], v[6:7], v[18:19]
	v_pk_mul_f32 v[10:11], v[8:9], v[20:21]
	s_waitcnt lgkmcnt(1)
	v_pk_mul_f32 v[14:15], v[2:3], v[22:23]
	v_pk_mul_f32 v[22:23], v[98:99], v[22:23]
	v_pk_fma_f32 v[112:113], v[6:7], v[18:19], v[14:15]
	s_waitcnt lgkmcnt(0)
	v_pk_mul_f32 v[114:115], v[30:31], v[18:19]
	v_pk_fma_f32 v[118:119], v[30:31], v[18:19], v[22:23]
	v_pk_mul_f32 v[4:5], v[4:5], v[24:25]
	v_pk_mul_f32 v[106:107], v[32:33], v[20:21]
	v_pk_mul_f32 v[24:25], v[100:101], v[24:25]
	ds_read_b128 v[98:101], v213 offset:18432
	v_cvt_pk_bf16_f32 v19, v106, v107
	ds_read_b128 v[106:109], v213 offset:19456
	v_pk_fma_f32 v[110:111], v[8:9], v[20:21], v[4:5]
	v_cvt_pk_bf16_f32 v5, v4, v5
	v_cvt_pk_bf16_f32 v3, v10, v11
	v_cvt_pk_bf16_f32 v4, v14, v15
	s_waitcnt lgkmcnt(0)
	v_pk_mul_f32 v[106:107], v[106:107], v[86:87]
	v_cvt_pk_bf16_f32 v2, v12, v13
	v_pk_mul_f32 v[120:121], v[98:99], v[82:83]
	v_pk_mul_f32 v[108:109], v[108:109], v[88:89]
	v_pk_fma_f32 v[98:99], v[98:99], v[82:83], v[106:107]
	v_mfma_f32_32x32x16_bf16 v[2:17], v[26:29], v[2:5], 0
	v_cvt_pk_bf16_f32 v18, v114, v115
	v_mul_f32_e32 v114, v100, v84
	v_mul_f32_e32 v115, v101, v85
	v_fma_f32 v100, v100, v84, v108
	v_fma_f32 v101, v101, v85, v109
	v_pk_add_f32 v[124:125], v[98:99], v[112:113]
	v_pk_add_f32 v[122:123], v[100:101], v[110:111]
	v_cvt_pk_bf16_f32 v101, v108, v109
	v_cvt_pk_bf16_f32 v100, v106, v107
	ds_read_b128 v[106:109], v213 offset:26624
	v_pk_fma_f32 v[116:117], v[32:33], v[20:21], v[24:25]
	v_cvt_pk_bf16_f32 v21, v24, v25
	v_cvt_pk_bf16_f32 v20, v22, v23
	ds_read_b128 v[110:113], v213 offset:27648
	v_cvt_pk_bf16_f32 v99, v114, v115
	v_mfma_f32_32x32x16_bf16 v[18:33], v[26:29], v[18:21], 0
	v_cvt_pk_bf16_f32 v98, v120, v121
	s_waitcnt lgkmcnt(1)
	v_mul_f32_e32 v114, v106, v82
	v_mul_f32_e32 v115, v107, v83
	s_waitcnt lgkmcnt(0)
	v_pk_mul_f32 v[86:87], v[110:111], v[86:87]
	v_pk_mul_f32 v[88:89], v[112:113], v[88:89]
	v_pk_fma_f32 v[82:83], v[106:107], v[82:83], v[86:87]
	v_mfma_f32_32x32x16_bf16 v[2:17], v[102:105], v[98:101], v[2:17]
	v_mul_f32_e32 v98, v108, v84
	v_mul_f32_e32 v99, v109, v85
	v_fma_f32 v84, v108, v84, v88
	v_fma_f32 v85, v109, v85, v89
	v_add_f32_e32 v108, v82, v118
	v_add_f32_e32 v109, v83, v119
	v_cvt_pk_bf16_f32 v83, v98, v99
	v_pk_add_f32 v[106:107], v[84:85], v[116:117]
	v_cvt_pk_bf16_f32 v85, v88, v89
	v_cvt_pk_bf16_f32 v84, v86, v87
	ds_read_b128 v[86:89], v213 offset:38912
	ds_read_b128 v[98:101], v213 offset:20480
	v_cvt_pk_bf16_f32 v82, v114, v115
	s_waitcnt lgkmcnt(0)
	v_pk_mul_f32 v[110:111], v[100:101], v[76:77]
	v_mfma_f32_32x32x16_bf16 v[18:33], v[102:105], v[82:85], v[18:33]
	ds_read_b128 v[82:85], v213 offset:21504
	ds_read_b128 v[102:105], v213 offset:28672
	v_mul_f32_e32 v112, v98, v74
	v_mul_f32_e32 v113, v99, v75
	s_waitcnt lgkmcnt(1)
	v_pk_mul_f32 v[84:85], v[84:85], v[80:81]
	v_pk_mul_f32 v[114:115], v[82:83], v[78:79]
	v_pk_fma_f32 v[82:83], v[100:101], v[76:77], v[84:85]
	v_cvt_pk_bf16_f32 v85, v84, v85
	v_pk_add_f32 v[116:117], v[82:83], v[122:123]
	v_cvt_pk_bf16_f32 v83, v110, v111
	v_cvt_pk_bf16_f32 v84, v114, v115
	v_cvt_pk_bf16_f32 v82, v112, v113
	v_pk_fma_f32 v[98:99], v[98:99], v[74:75], v[114:115]
	s_waitcnt lgkmcnt(0)
	v_pk_mul_f32 v[112:113], v[102:103], v[74:75]
	v_mfma_f32_32x32x16_bf16 v[2:17], v[86:89], v[82:85], v[2:17]
	ds_read_b128 v[82:85], v213 offset:29696
	v_add_f32_e32 v118, v98, v124
	v_add_f32_e32 v119, v99, v125
	v_mul_f32_e32 v110, v104, v76
	v_mul_f32_e32 v111, v105, v77
	ds_read_b128 v[98:101], v213 offset:39936
	s_waitcnt lgkmcnt(1)
	v_pk_mul_f32 v[78:79], v[82:83], v[78:79]
	v_pk_mul_f32 v[80:81], v[84:85], v[80:81]
	v_pk_fma_f32 v[74:75], v[102:103], v[74:75], v[78:79]
	v_pk_fma_f32 v[76:77], v[104:105], v[76:77], v[80:81]
	v_pk_add_f32 v[104:105], v[74:75], v[108:109]
	v_pk_add_f32 v[102:103], v[76:77], v[106:107]
	v_cvt_pk_bf16_f32 v77, v80, v81
	v_cvt_pk_bf16_f32 v76, v78, v79
	ds_read_b128 v[78:81], v213 offset:22528
	ds_read_b128 v[82:85], v213 offset:23552
	v_cvt_pk_bf16_f32 v75, v110, v111
	v_cvt_pk_bf16_f32 v74, v112, v113
	s_waitcnt lgkmcnt(0)
	v_pk_mul_f32 v[82:83], v[82:83], v[70:71]
	v_mfma_f32_32x32x16_bf16 v[18:33], v[86:89], v[74:77], v[18:33]
	v_mul_f32_e32 v74, v80, v68
	v_mul_f32_e32 v75, v81, v69
	v_mul_f32_e32 v76, v84, v72
	v_mul_f32_e32 v77, v85, v73
	v_mul_f32_e32 v86, v78, v66
	v_mul_f32_e32 v87, v79, v67
	v_pk_fma_f32 v[80:81], v[80:81], v[68:69], v[76:77]
	v_pk_fma_f32 v[78:79], v[78:79], v[66:67], v[82:83]
	v_cvt_pk_bf16_f32 v75, v74, v75
	v_pk_add_f32 v[88:89], v[80:81], v[116:117]
	v_pk_add_f32 v[106:107], v[78:79], v[118:119]
	ds_read_b128 v[78:81], v213 offset:30720
	v_cvt_pk_bf16_f32 v77, v76, v77
	v_cvt_pk_bf16_f32 v76, v82, v83
	ds_read_b128 v[82:85], v213 offset:31744
	v_cvt_pk_bf16_f32 v74, v86, v87
	s_waitcnt lgkmcnt(0)
	v_pk_mul_f32 v[72:73], v[84:85], v[72:73]
	v_mfma_f32_32x32x16_bf16 v[2:17], v[98:101], v[74:77], v[2:17]
	v_mul_f32_e32 v74, v80, v68
	v_mul_f32_e32 v75, v81, v69
	v_fma_f32 v68, v80, v68, v72
	v_fma_f32 v69, v81, v69, v73
	v_mul_f32_e32 v70, v82, v70
	v_mul_f32_e32 v71, v83, v71
	v_pk_add_f32 v[84:85], v[68:69], v[102:103]
	v_cvt_pk_bf16_f32 v69, v72, v73
	v_pk_mov_b32 v[72:73], v[96:97], v[94:95] op_sel:[1,0]
	v_mov_b32_e32 v97, v95
	v_pk_add_f32 v[72:73], v[72:73], v[96:97]
	v_pk_mul_f32 v[76:77], v[78:79], v[66:67]
	v_pk_fma_f32 v[66:67], v[78:79], v[66:67], v[70:71]
	v_pk_add_f32 v[72:73], v[72:73], v[72:73] op_sel:[0,1] op_sel_hi:[1,0]
	v_pk_add_f32 v[86:87], v[66:67], v[104:105]
	v_mov_b32_e32 v66, v72
	s_nop 1
	v_permlane32_swap_b32_e32 v72, v66
	v_add_f32_e32 v66, v72, v66
	v_cvt_pk_bf16_f32 v67, v74, v75
	v_rcp_f32_e32 v74, v66
	v_cvt_pk_bf16_f32 v68, v70, v71
	v_cvt_pk_bf16_f32 v66, v76, v77
	v_pk_mul_f32 v[70:71], v[46:47], v[74:75] op_sel_hi:[1,0]
	s_nop 0
	v_mfma_f32_32x32x16_bf16 v[18:33], v[98:101], v[66:69], v[18:33]
	v_mul_f32_e32 v66, v42, v74
	v_mul_f32_e32 v67, v43, v74
	v_pk_mov_b32 v[42:43], v[92:93], v[90:91] op_sel:[1,0]
	v_mov_b32_e32 v93, v91
	v_pk_add_f32 v[42:43], v[42:43], v[92:93]
	v_pk_mul_f32 v[68:69], v[44:45], v[74:75] op_sel_hi:[1,0]
	v_pk_add_f32 v[42:43], v[42:43], v[42:43] op_sel:[0,1] op_sel_hi:[1,0]
	v_pk_mov_b32 v[44:45], v[106:107], v[88:89] op_sel:[1,0]
	v_mov_b32_e32 v43, v42
	s_nop 1
	v_permlane32_swap_b32_e32 v42, v43
	v_add_f32_e32 v42, v42, v43
	v_rcp_f32_e32 v42, v42
	v_mov_b32_e32 v107, v89
	v_pk_add_f32 v[44:45], v[44:45], v[106:107]
	v_pk_mul_f32 v[72:73], v[48:49], v[74:75] op_sel_hi:[1,0]
	v_pk_add_f32 v[44:45], v[44:45], v[44:45] op_sel:[0,1] op_sel_hi:[1,0]
	v_pk_mul_f32 v[36:37], v[36:37], v[74:75] op_sel_hi:[1,0]
	v_pk_mul_f32 v[38:39], v[38:39], v[74:75] op_sel_hi:[1,0]
	v_pk_mul_f32 v[40:41], v[40:41], v[74:75] op_sel_hi:[1,0]
	v_pk_mul_f32 v[34:35], v[34:35], v[74:75] op_sel_hi:[1,0]
	v_pk_mul_f32 v[74:75], v[58:59], v[42:43] op_sel_hi:[1,0]
	v_pk_mul_f32 v[78:79], v[60:61], v[42:43] op_sel_hi:[1,0]
	v_pk_mul_f32 v[80:81], v[62:63], v[42:43] op_sel_hi:[1,0]
	v_pk_mul_f32 v[82:83], v[64:65], v[42:43] op_sel_hi:[1,0]
	v_pk_mul_f32 v[92:93], v[52:53], v[42:43] op_sel_hi:[1,0]
	v_mov_b32_e32 v43, v44
	s_nop 1
	v_permlane32_swap_b32_e32 v44, v43
	v_add_f32_e32 v43, v44, v43
	v_rcp_f32_e32 v76, v43
	v_pk_mul_f32 v[96:97], v[54:55], v[42:43] op_sel_hi:[1,0]
	v_pk_mul_f32 v[94:95], v[56:57], v[42:43] op_sel_hi:[1,0]
	v_pk_mul_f32 v[98:99], v[50:51], v[42:43] op_sel_hi:[1,0]
	v_pk_mul_f32 v[100:101], v[4:5], v[76:77] op_sel_hi:[1,0]
	v_pk_mov_b32 v[4:5], v[86:87], v[84:85] op_sel:[1,0]
	v_mov_b32_e32 v87, v85
	v_pk_add_f32 v[4:5], v[4:5], v[86:87]
	v_pk_mul_f32 v[102:103], v[6:7], v[76:77] op_sel_hi:[1,0]
	v_pk_add_f32 v[104:105], v[4:5], v[4:5] op_sel:[0,1] op_sel_hi:[1,0]
	v_cvt_pk_bf16_f32 v7, v40, v41
	ds_read_b128 v[84:87], v150 offset:52224
	ds_read_b128 v[50:53], v150 offset:35840
	ds_read_b128 v[54:57], v150 offset:36864
	ds_read_b128 v[58:61], v150 offset:37888
	ds_read_b128 v[62:65], v150 offset:38912
	v_cvt_pk_bf16_f32 v6, v38, v39
	v_cvt_pk_bf16_f32 v5, v36, v37
	v_cvt_pk_bf16_f32 v4, v34, v35
	ds_read_b128 v[88:91], v150 offset:53248
	ds_read_b128 v[34:37], v150 offset:39936
	ds_read_b128 v[38:41], v150 offset:40960
	ds_read_b128 v[42:45], v150 offset:41984
	ds_read_b128 v[46:49], v150 offset:43008
	v_cvt_pk_bf16_f32 v95, v94, v95
	v_cvt_pk_bf16_f32 v94, v96, v97
	v_cvt_pk_bf16_f32 v93, v92, v93
	v_cvt_pk_bf16_f32 v92, v98, v99
	s_waitcnt lgkmcnt(5)
	v_mfma_f32_32x32x16_bf16 v[50:65], v[84:87], v[4:7], v[50:65]
	v_mul_f32_e32 v10, v10, v76
	v_mul_f32_e32 v11, v11, v76
	v_mul_f32_e32 v12, v12, v76
	v_mul_f32_e32 v13, v13, v76
	v_mul_f32_e32 v8, v8, v76
	v_mul_f32_e32 v9, v9, v76
	v_mov_b32_e32 v77, v104
	s_nop 1
	v_permlane32_swap_b32_e32 v104, v77
	v_cvt_pk_bf16_f32 v73, v72, v73
	s_waitcnt lgkmcnt(0)
	v_mfma_f32_32x32x16_bf16 v[34:49], v[84:87], v[92:95], v[34:49]
	v_cvt_pk_bf16_f32 v72, v70, v71
	v_cvt_pk_bf16_f32 v70, v66, v67
	v_add_f32_e32 v66, v104, v77
	v_cvt_pk_bf16_f32 v71, v68, v69
	v_rcp_f32_e32 v104, v66
	v_cvt_pk_bf16_f32 v69, v82, v83
	v_cvt_pk_bf16_f32 v68, v80, v81
	v_cvt_pk_bf16_f32 v67, v78, v79
	v_cvt_pk_bf16_f32 v66, v74, v75
	ds_read_b128 v[78:81], v150 offset:54272
	v_mfma_f32_32x32x16_bf16 v[50:65], v[88:91], v[70:73], v[50:65]
	v_mul_f32_e32 v2, v2, v76
	v_mul_f32_e32 v3, v3, v76
	v_mul_f32_e32 v20, v20, v104
	v_mul_f32_e32 v21, v21, v104
	v_cvt_pk_bf16_f32 v85, v8, v9
	v_cvt_pk_bf16_f32 v82, v2, v3
	v_pk_mul_f32 v[2:3], v[22:23], v[104:105] op_sel_hi:[1,0]
	v_pk_mul_f32 v[8:9], v[24:25], v[104:105] op_sel_hi:[1,0]
	v_pk_mul_f32 v[18:19], v[18:19], v[104:105] op_sel_hi:[1,0]
	v_mfma_f32_32x32x16_bf16 v[34:49], v[88:91], v[66:69], v[34:49]
	v_cvt_pk_bf16_f32 v84, v102, v103
	v_cvt_pk_bf16_f32 v83, v100, v101
	ds_read_b128 v[86:89], v150 offset:55296
	v_cvt_pk_bf16_f32 v99, v8, v9
	v_cvt_pk_bf16_f32 v98, v2, v3
	v_cvt_pk_bf16_f32 v97, v20, v21
	v_cvt_pk_bf16_f32 v96, v18, v19
	s_waitcnt lgkmcnt(1)
	v_mfma_f32_32x32x16_bf16 v[50:65], v[78:81], v[82:85], v[50:65]
	v_mul_f32_e32 v2, v14, v76
	v_mul_f32_e32 v3, v15, v76
	v_mul_f32_e32 v8, v16, v76
	v_mul_f32_e32 v9, v17, v76
	v_mul_f32_e32 v14, v26, v104
	v_mul_f32_e32 v15, v27, v104
	v_cvt_pk_bf16_f32 v77, v8, v9
	v_cvt_pk_bf16_f32 v76, v2, v3
	v_cvt_pk_bf16_f32 v74, v10, v11
	v_pk_mul_f32 v[2:3], v[28:29], v[104:105] op_sel_hi:[1,0]
	v_mfma_f32_32x32x16_bf16 v[34:49], v[78:81], v[96:99], v[34:49]
	v_mul_f32_e32 v8, v30, v104
	v_mul_f32_e32 v9, v31, v104
	v_mul_f32_e32 v10, v32, v104
	v_mul_f32_e32 v11, v33, v104
	v_cvt_pk_bf16_f32 v75, v12, v13
	v_cvt_pk_bf16_f32 v81, v10, v11
	v_cvt_pk_bf16_f32 v80, v8, v9
	v_cvt_pk_bf16_f32 v79, v2, v3
	v_cvt_pk_bf16_f32 v78, v14, v15
	s_waitcnt lgkmcnt(0)
	v_mfma_f32_32x32x16_bf16 v[50:65], v[86:89], v[74:77], v[50:65]
	v_mfma_f32_32x32x16_bf16 v[34:49], v[86:89], v[78:81], v[34:49]
	ds_read_b128 v[86:89], v150 offset:56320
	ds_read_b128 v[18:21], v150 offset:44032
	ds_read_b128 v[22:25], v150 offset:45056
	ds_read_b128 v[26:29], v150 offset:46080
	ds_read_b128 v[30:33], v150 offset:47104
	ds_read_b128 v[100:103], v150 offset:57344
	s_waitcnt lgkmcnt(1)
	v_mfma_f32_32x32x16_bf16 v[18:33], v[86:89], v[4:7], v[18:33]
	ds_read_b128 v[2:5], v150 offset:48128
	ds_read_b128 v[6:9], v150 offset:49152
	ds_read_b128 v[10:13], v150 offset:50176
	ds_read_b128 v[14:17], v150 offset:51200
	s_waitcnt lgkmcnt(0)
	v_mfma_f32_32x32x16_bf16 v[2:17], v[86:89], v[92:95], v[2:17]
	v_mfma_f32_32x32x16_bf16 v[18:33], v[100:103], v[70:73], v[18:33]
	v_mfma_f32_32x32x16_bf16 v[2:17], v[100:103], v[66:69], v[2:17]
	ds_read_b128 v[66:69], v150 offset:58368
	ds_read_b128 v[70:73], v150 offset:59392
	s_waitcnt lgkmcnt(1)
	v_mfma_f32_32x32x16_bf16 v[18:33], v[66:69], v[82:85], v[18:33]
	v_mfma_f32_32x32x16_bf16 v[2:17], v[66:69], v[96:99], v[2:17]
	s_waitcnt lgkmcnt(0)
	v_mfma_f32_32x32x16_bf16 v[18:33], v[70:73], v[74:77], v[18:33]
	v_mfma_f32_32x32x16_bf16 v[2:17], v[70:73], v[78:81], v[2:17]
	s_nop 10
	v_mul_f32_e32 v66, v22, v22
	v_mul_f32_e32 v67, v23, v23
	v_mul_f32_e32 v68, v30, v30
	v_mul_f32_e32 v69, v31, v31
	v_mul_f32_e32 v70, v24, v24
	v_mul_f32_e32 v71, v25, v25
	v_pk_mul_f32 v[72:73], v[32:33], v[32:33]
	v_pk_mul_f32 v[74:75], v[20:21], v[20:21]
	v_pk_mul_f32 v[76:77], v[28:29], v[28:29]
	v_pk_mul_f32 v[78:79], v[26:27], v[26:27]
	v_pk_mul_f32 v[80:81], v[18:19], v[18:19]
	v_pk_fma_f32 v[78:79], v[58:59], v[58:59], v[78:79]
	v_pk_fma_f32 v[76:77], v[60:61], v[60:61], v[76:77]
	v_pk_fma_f32 v[74:75], v[52:53], v[52:53], v[74:75]
	v_pk_fma_f32 v[72:73], v[64:65], v[64:65], v[72:73]
	v_pk_fma_f32 v[70:71], v[56:57], v[56:57], v[70:71]
	v_pk_fma_f32 v[68:69], v[62:63], v[62:63], v[68:69]
	v_pk_fma_f32 v[66:67], v[54:55], v[54:55], v[66:67]
	v_pk_fma_f32 v[80:81], v[50:51], v[50:51], v[80:81]
	v_pk_add_f32 v[66:67], v[66:67], v[68:69]
	v_pk_add_f32 v[68:69], v[70:71], v[72:73]
	v_pk_add_f32 v[70:71], v[74:75], v[76:77]
	v_pk_add_f32 v[72:73], v[80:81], v[78:79]
	v_pk_add_f32 v[68:69], v[70:71], v[68:69]
	v_pk_add_f32 v[66:67], v[72:73], v[66:67]
	v_pk_mul_f32 v[72:73], v[14:15], v[14:15]
	v_pk_mov_b32 v[70:71], v[66:67], v[68:69] op_sel:[1,0]
	v_mov_b32_e32 v67, v69
	v_pk_add_f32 v[66:67], v[70:71], v[66:67]
	v_pk_mul_f32 v[70:71], v[6:7], v[6:7]
	v_pk_mul_f32 v[74:75], v[8:9], v[8:9]
	v_pk_mul_f32 v[76:77], v[16:17], v[16:17]
	v_pk_mul_f32 v[78:79], v[4:5], v[4:5]
	v_pk_mul_f32 v[80:81], v[12:13], v[12:13]
	v_pk_mul_f32 v[82:83], v[10:11], v[10:11]
	v_pk_mul_f32 v[84:85], v[2:3], v[2:3]
	v_pk_fma_f32 v[82:83], v[42:43], v[42:43], v[82:83]
	v_pk_fma_f32 v[80:81], v[44:45], v[44:45], v[80:81]
	v_pk_fma_f32 v[78:79], v[36:37], v[36:37], v[78:79]
	v_pk_fma_f32 v[76:77], v[48:49], v[48:49], v[76:77]
	v_pk_fma_f32 v[74:75], v[40:41], v[40:41], v[74:75]
	v_pk_fma_f32 v[72:73], v[46:47], v[46:47], v[72:73]
	v_pk_fma_f32 v[70:71], v[38:39], v[38:39], v[70:71]
	v_pk_fma_f32 v[84:85], v[34:35], v[34:35], v[84:85]
	v_pk_add_f32 v[70:71], v[70:71], v[72:73]
	v_pk_add_f32 v[72:73], v[74:75], v[76:77]
	v_pk_add_f32 v[74:75], v[78:79], v[80:81]
	v_pk_add_f32 v[76:77], v[84:85], v[82:83]
	v_pk_add_f32 v[72:73], v[74:75], v[72:73]
	v_pk_add_f32 v[70:71], v[76:77], v[70:71]
	v_pk_add_f32 v[66:67], v[66:67], v[66:67] op_sel:[0,1] op_sel_hi:[1,0]
	v_pk_mov_b32 v[74:75], v[70:71], v[72:73] op_sel:[1,0]
	v_mov_b32_e32 v71, v73
	v_pk_add_f32 v[70:71], v[74:75], v[70:71]
	v_mov_b32_e32 v69, v66
	v_pk_add_f32 v[70:71], v[70:71], v[70:71] op_sel:[0,1] op_sel_hi:[1,0]
	s_nop 0
	v_permlane32_swap_b32_e32 v66, v69
	v_mov_b32_e32 v68, v70
	s_nop 1
	v_permlane32_swap_b32_e32 v70, v68
	v_mov_b32_e32 v71, v66
	v_pk_add_f32 v[66:67], v[70:71], v[68:69]
	v_pk_fma_f32 v[66:67], v[66:67], s[0:1], v[152:153] op_sel_hi:[1,0,0]
	s_mov_b32 s1, 0x800000
	v_mul_f32_e32 v68, 0x4b800000, v67
	v_cmp_gt_f32_e32 vcc, s1, v67
	s_nop 1
	v_cndmask_b32_e32 v67, v67, v68, vcc
	v_rsq_f32_e32 v67, v67
	s_nop 0
	v_mul_f32_e32 v68, 0x45800000, v67
	v_cndmask_b32_e32 v68, v67, v68, vcc
	v_pk_mul_f32 v[158:159], v[50:51], v[68:69] op_sel_hi:[1,0]
	v_pk_mul_f32 v[50:51], v[18:19], v[68:69] op_sel_hi:[1,0]
	v_mul_f32_e32 v18, 0x4b800000, v66
	v_cmp_gt_f32_e32 vcc, s1, v66
	v_pk_mul_f32 v[80:81], v[60:61], v[68:69] op_sel_hi:[1,0]
	v_pk_mul_f32 v[60:61], v[28:29], v[68:69] op_sel_hi:[1,0]
	v_cndmask_b32_e32 v18, v66, v18, vcc
	v_rsq_f32_e32 v18, v18
	v_pk_mul_f32 v[78:79], v[58:59], v[68:69] op_sel_hi:[1,0]
	v_pk_mul_f32 v[160:161], v[52:53], v[68:69] op_sel_hi:[1,0]
	v_pk_mul_f32 v[82:83], v[54:55], v[68:69] op_sel_hi:[1,0]
	v_mul_f32_e32 v19, 0x45800000, v18
	v_cndmask_b32_e32 v28, v18, v19, vcc
	v_pk_mul_f32 v[168:169], v[56:57], v[68:69] op_sel_hi:[1,0]
	v_pk_mul_f32 v[58:59], v[26:27], v[68:69] op_sel_hi:[1,0]
	v_pk_mul_f32 v[52:53], v[20:21], v[68:69] op_sel_hi:[1,0]
	v_pk_mul_f32 v[54:55], v[22:23], v[68:69] op_sel_hi:[1,0]
	v_pk_mul_f32 v[56:57], v[24:25], v[68:69] op_sel_hi:[1,0]
	v_pk_mul_f32 v[18:19], v[42:43], v[28:29] op_sel_hi:[1,0]
	v_pk_mul_f32 v[20:21], v[44:45], v[28:29] op_sel_hi:[1,0]
	v_pk_mul_f32 v[22:23], v[46:47], v[28:29] op_sel_hi:[1,0]
	v_pk_mul_f32 v[26:27], v[48:49], v[28:29] op_sel_hi:[1,0]
	v_pk_mul_f32 v[162:163], v[34:35], v[28:29] op_sel_hi:[1,0]
	v_pk_mul_f32 v[164:165], v[36:37], v[28:29] op_sel_hi:[1,0]
	v_pk_mul_f32 v[166:167], v[38:39], v[28:29] op_sel_hi:[1,0]
	v_pk_mul_f32 v[24:25], v[40:41], v[28:29] op_sel_hi:[1,0]
	v_pk_mul_f32 v[104:105], v[2:3], v[28:29] op_sel_hi:[1,0]
	v_pk_mul_f32 v[112:113], v[4:5], v[28:29] op_sel_hi:[1,0]
	s_nop 0
	s_nop 0
	ds_read_b128 v[2:5], v150 offset:60416
	ds_read_b128 v[34:37], v174 offset:32768
	ds_read_b128 v[38:41], v174 offset:32800
	ds_read_b128 v[42:45], v174 offset:32832
	ds_read_b128 v[46:49], v174 offset:32864
	v_cvt_pk_bf16_f32 v129, v168, v169
	v_cvt_pk_bf16_f32 v128, v82, v83
	v_cvt_pk_bf16_f32 v127, v160, v161
	v_cvt_pk_bf16_f32 v126, v158, v159
	v_cvt_pk_bf16_f32 v137, v24, v25
	v_cvt_pk_bf16_f32 v136, v166, v167
	v_cvt_pk_bf16_f32 v135, v164, v165
	s_waitcnt lgkmcnt(0)
	v_mfma_f32_32x32x16_bf16 v[86:101], v[2:5], v[126:129], v[34:49]
	v_cvt_pk_bf16_f32 v134, v162, v163
	v_mul_f32_e32 v84, v62, v68
	v_mul_f32_e32 v85, v63, v68
	v_mul_f32_e32 v170, v64, v68
	v_mul_f32_e32 v171, v65, v68
	v_pk_mul_f32 v[62:63], v[30:31], v[68:69] op_sel_hi:[1,0]
	v_pk_mul_f32 v[64:65], v[32:33], v[68:69] op_sel_hi:[1,0]
	v_pk_mul_f32 v[116:117], v[6:7], v[28:29] op_sel_hi:[1,0]
	v_pk_mul_f32 v[154:155], v[8:9], v[28:29] op_sel_hi:[1,0]
	v_mfma_f32_32x32x16_bf16 v[34:49], v[2:5], v[134:137], v[34:49]
	ds_read_b128 v[6:9], v150 offset:61440
	ds_read_b128 v[66:69], v174 offset:32896
	ds_read_b128 v[106:109], v150 offset:64512
	v_cvt_pk_bf16_f32 v125, v170, v171
	v_cvt_pk_bf16_f32 v124, v84, v85
	v_cvt_pk_bf16_f32 v123, v80, v81
	v_cvt_pk_bf16_f32 v122, v78, v79
	v_cvt_pk_bf16_f32 v149, v26, v27
	v_cvt_pk_bf16_f32 v148, v22, v23
	v_cvt_pk_bf16_f32 v147, v20, v21
	v_cvt_pk_bf16_f32 v146, v18, v19
	s_waitcnt lgkmcnt(2)
	v_mfma_f32_32x32x16_bf16 v[86:101], v[6:9], v[122:125], v[86:101]
	v_mul_f32_e32 v102, v10, v28
	v_mul_f32_e32 v103, v11, v28
	v_mul_f32_e32 v110, v12, v28
	v_mul_f32_e32 v111, v13, v28
	v_mul_f32_e32 v114, v14, v28
	v_mul_f32_e32 v115, v15, v28
	v_pk_mul_f32 v[156:157], v[16:17], v[28:29] op_sel_hi:[1,0]
	ds_read_b128 v[176:179], v174 offset:33536
	ds_read_b128 v[180:183], v174 offset:33568
	ds_read_b128 v[184:187], v174 offset:33600
	ds_read_b128 v[28:31], v174 offset:33632
	ds_read_b128 v[188:191], v174 offset:33792
	ds_read_b128 v[192:195], v174 offset:33824
	ds_read_b128 v[196:199], v174 offset:33856
	ds_read_b128 v[200:203], v174 offset:33888
	ds_read_b128 v[204:207], v150 offset:62464
	v_cvt_pk_bf16_f32 v133, v56, v57
	v_mfma_f32_32x32x16_bf16 v[34:49], v[6:9], v[146:149], v[34:49]
	v_cvt_pk_bf16_f32 v132, v54, v55
	v_cvt_pk_bf16_f32 v131, v52, v53
	v_cvt_pk_bf16_f32 v130, v50, v51
	ds_read_b128 v[70:73], v174 offset:33664
	ds_read_b128 v[74:77], v174 offset:33920
	ds_read_b128 v[208:211], v150 offset:63488
	v_cvt_pk_bf16_f32 v145, v154, v155
	v_cvt_pk_bf16_f32 v144, v116, v117
	v_cvt_pk_bf16_f32 v143, v112, v113
	v_cvt_pk_bf16_f32 v142, v104, v105
	s_waitcnt lgkmcnt(3)
	v_mfma_f32_32x32x16_bf16 v[86:101], v[204:207], v[130:133], v[86:101]
	v_cvt_pk_bf16_f32 v121, v64, v65
	v_cvt_pk_bf16_f32 v120, v62, v63
	v_cvt_pk_bf16_f32 v119, v60, v61
	v_cvt_pk_bf16_f32 v118, v58, v59
	v_cvt_pk_bf16_f32 v141, v156, v157
	v_cvt_pk_bf16_f32 v140, v114, v115
	v_cvt_pk_bf16_f32 v139, v110, v111
	v_mfma_f32_32x32x16_bf16 v[34:49], v[204:207], v[142:145], v[34:49]
	v_cvt_pk_bf16_f32 v138, v102, v103
	v_fma_f32 v16, v30, v170, v202
	v_fma_f32 v17, v31, v171, v203
	v_fma_f32 v14, v28, v84, v200
	v_fma_f32 v15, v29, v85, v201
	v_pk_fma_f32 v[12:13], v[186:187], v[80:81], v[198:199]
	v_pk_fma_f32 v[10:11], v[184:185], v[78:79], v[196:197]
	v_pk_fma_f32 v[8:9], v[182:183], v[168:169], v[194:195]
	s_waitcnt lgkmcnt(0)
	v_mfma_f32_32x32x16_bf16 v[86:101], v[208:211], v[118:121], v[86:101]
	v_fma_f32 v6, v180, v82, v192
	v_fma_f32 v7, v181, v83, v193
	ds_read_b128 v[78:81], v174 offset:33760
	ds_read_b128 v[82:85], v174 offset:33248
	v_fma_f32 v4, v178, v160, v190
	v_fma_f32 v5, v179, v161, v191
	v_pk_fma_f32 v[2:3], v[176:177], v[158:159], v[188:189]
	v_pk_fma_f32 v[32:33], v[30:31], v[26:27], v[202:203]
	v_pk_fma_f32 v[30:31], v[28:29], v[22:23], v[200:201]
	v_pk_fma_f32 v[28:29], v[186:187], v[20:21], v[198:199]
	v_pk_fma_f32 v[26:27], v[184:185], v[18:19], v[196:197]
	v_pk_fma_f32 v[24:25], v[182:183], v[24:25], v[194:195]
	v_pk_fma_f32 v[22:23], v[180:181], v[166:167], v[192:193]
	v_pk_fma_f32 v[20:21], v[178:179], v[164:165], v[190:191]
	v_pk_fma_f32 v[18:19], v[176:177], v[162:163], v[188:189]
	ds_read_b128 v[158:161], v174 offset:33696
	ds_read_b128 v[162:165], v174 offset:33728
	ds_read_b128 v[166:169], v174 offset:33952
	ds_read_b128 v[176:179], v174 offset:33984
	ds_read_b128 v[180:183], v174 offset:34016
	ds_read_b128 v[184:187], v212 offset:11264
	v_mfma_f32_32x32x16_bf16 v[34:49], v[208:211], v[138:141], v[34:49]
	v_cvt_pk_bf16_f32 v86, v86, v87
	v_cvt_pk_bf16_f32 v87, v88, v89
	v_cvt_pk_bf16_f32 v88, v90, v91
	v_cvt_pk_bf16_f32 v89, v92, v93
	ds_read_b128 v[90:93], v212 offset:12288
	v_pk_max_i16 v86, v86, 0
	v_pk_max_i16 v87, v87, 0
	v_pk_max_i16 v88, v88, 0
	v_pk_max_i16 v89, v89, 0
	s_nop 1
	s_nop 0
	v_cvt_pk_bf16_f32 v188, v34, v35
	v_cvt_pk_bf16_f32 v189, v36, v37
	v_cvt_pk_bf16_f32 v190, v38, v39
	v_cvt_pk_bf16_f32 v191, v40, v41
	s_waitcnt lgkmcnt(1)
	v_mfma_f32_32x32x16_bf16 v[2:17], v[184:187], v[86:89], v[2:17]
	v_pk_max_i16 v188, v188, 0
	v_pk_max_i16 v189, v189, 0
	v_pk_max_i16 v190, v190, 0
	v_pk_max_i16 v191, v191, 0
	v_cvt_pk_bf16_f32 v94, v94, v95
	v_cvt_pk_bf16_f32 v95, v96, v97
	v_cvt_pk_bf16_f32 v96, v98, v99
	v_cvt_pk_bf16_f32 v97, v100, v101
	v_cvt_pk_bf16_f32 v98, v42, v43
	v_cvt_pk_bf16_f32 v99, v44, v45
	v_mfma_f32_32x32x16_bf16 v[18:33], v[184:187], v[188:191], v[18:33]
	ds_read_b128 v[184:187], v212 offset:19456
	v_cvt_pk_bf16_f32 v100, v46, v47
	v_cvt_pk_bf16_f32 v101, v48, v49
	v_fma_f32 v64, v80, v64, v182
	v_fma_f32 v65, v81, v65, v183
	v_pk_fma_f32 v[62:63], v[78:79], v[62:63], v[180:181]
	v_pk_fma_f32 v[60:61], v[164:165], v[60:61], v[178:179]
	v_pk_fma_f32 v[58:59], v[162:163], v[58:59], v[176:177]
	v_pk_max_i16 v94, v94, 0
	v_pk_max_i16 v95, v95, 0
	v_pk_max_i16 v96, v96, 0
	v_pk_max_i16 v97, v97, 0
	v_pk_max_i16 v98, v98, 0
	v_pk_max_i16 v99, v99, 0
	v_pk_max_i16 v100, v100, 0
	v_pk_max_i16 v101, v101, 0
	v_pk_fma_f32 v[56:57], v[160:161], v[56:57], v[168:169]
	s_waitcnt lgkmcnt(1)
	v_mfma_f32_32x32x16_bf16 v[2:17], v[90:93], v[94:97], v[2:17]
	v_fma_f32 v54, v158, v54, v166
	v_fma_f32 v55, v159, v55, v167
	v_fma_f32 v52, v72, v52, v76
	v_fma_f32 v53, v73, v53, v77
	v_fma_f32 v50, v70, v50, v74
	v_fma_f32 v51, v71, v51, v75
	v_pk_fma_f32 v[48:49], v[80:81], v[156:157], v[182:183]
	v_pk_fma_f32 v[46:47], v[78:79], v[114:115], v[180:181]
	v_pk_fma_f32 v[44:45], v[164:165], v[110:111], v[178:179]
	v_pk_fma_f32 v[42:43], v[162:163], v[102:103], v[176:177]
	v_mfma_f32_32x32x16_bf16 v[18:33], v[90:93], v[98:101], v[18:33]
	ds_read_b128 v[90:93], v212 offset:20480
	v_fma_f32 v40, v160, v154, v168
	v_fma_f32 v41, v161, v155, v169
	v_fma_f32 v38, v158, v116, v166
	v_fma_f32 v39, v159, v117, v167
	v_pk_fma_f32 v[36:37], v[72:73], v[112:113], v[76:77]
	v_pk_fma_f32 v[34:35], v[70:71], v[104:105], v[74:75]
	s_waitcnt lgkmcnt(1)
	v_mfma_f32_32x32x16_bf16 v[50:65], v[184:187], v[86:89], v[50:65]
	ds_read_b128 v[70:73], v174 offset:32928
	ds_read_b128 v[74:77], v174 offset:32960
	ds_read_b128 v[78:81], v174 offset:32992
	ds_read_b128 v[86:89], v174 offset:33024
	ds_read_b128 v[110:113], v212 offset:1024
	v_mfma_f32_32x32x16_bf16 v[34:49], v[184:187], v[188:191], v[34:49]
	s_waitcnt lgkmcnt(5)
	v_mfma_f32_32x32x16_bf16 v[50:65], v[90:93], v[94:97], v[50:65]
	v_mfma_f32_32x32x16_bf16 v[34:49], v[90:93], v[98:101], v[34:49]
	s_waitcnt lgkmcnt(2)
	v_mfma_f32_32x32x16_bf16 v[90:105], v[106:109], v[126:129], v[66:81]
	v_mfma_f32_32x32x16_bf16 v[66:81], v[106:109], v[134:137], v[66:81]
	ds_read_b128 v[106:109], v212 offset:0
	s_waitcnt lgkmcnt(0)
	v_mfma_f32_32x32x16_bf16 v[90:105], v[106:109], v[122:125], v[90:105]
	v_mfma_f32_32x32x16_bf16 v[66:81], v[106:109], v[146:149], v[66:81]
	ds_read_b128 v[106:109], v212 offset:2048
	v_mfma_f32_32x32x16_bf16 v[90:105], v[110:113], v[130:133], v[90:105]
	v_mfma_f32_32x32x16_bf16 v[66:81], v[110:113], v[142:145], v[66:81]
	ds_read_b128 v[110:113], v212 offset:13312
	s_waitcnt lgkmcnt(1)
	v_mfma_f32_32x32x16_bf16 v[90:105], v[106:109], v[118:121], v[90:105]
	v_mfma_f32_32x32x16_bf16 v[66:81], v[106:109], v[138:141], v[66:81]
	s_nop 10
	v_cvt_pk_bf16_f32 v90, v90, v91
	v_cvt_pk_bf16_f32 v91, v92, v93
	v_cvt_pk_bf16_f32 v92, v94, v95
	v_cvt_pk_bf16_f32 v94, v98, v99
	v_cvt_pk_bf16_f32 v95, v100, v101
	ds_read_b128 v[98:101], v212 offset:21504
	v_cvt_pk_bf16_f32 v66, v66, v67
	v_cvt_pk_bf16_f32 v67, v68, v69
	v_cvt_pk_bf16_f32 v68, v70, v71
	v_cvt_pk_bf16_f32 v93, v96, v97
	v_cvt_pk_bf16_f32 v69, v72, v73
	ds_read_b128 v[70:73], v212 offset:14336
	v_pk_max_i16 v90, v90, 0
	v_pk_max_i16 v91, v91, 0
	v_pk_max_i16 v92, v92, 0
	v_pk_max_i16 v93, v93, 0
	v_pk_max_i16 v66, v66, 0
	v_pk_max_i16 v67, v67, 0
	v_pk_max_i16 v68, v68, 0
	v_pk_max_i16 v69, v69, 0
	v_cvt_pk_bf16_f32 v96, v102, v103
	s_waitcnt lgkmcnt(2)
	v_mfma_f32_32x32x16_bf16 v[2:17], v[110:113], v[90:93], v[2:17]
	v_cvt_pk_bf16_f32 v97, v104, v105
	v_cvt_pk_bf16_f32 v74, v74, v75
	v_cvt_pk_bf16_f32 v75, v76, v77
	v_cvt_pk_bf16_f32 v76, v78, v79
	v_cvt_pk_bf16_f32 v77, v80, v81
	v_pk_max_i16 v94, v94, 0
	v_pk_max_i16 v95, v95, 0
	v_pk_max_i16 v96, v96, 0
	v_pk_max_i16 v97, v97, 0
	v_pk_max_i16 v74, v74, 0
	v_pk_max_i16 v75, v75, 0
	v_pk_max_i16 v76, v76, 0
	v_pk_max_i16 v77, v77, 0
	v_mfma_f32_32x32x16_bf16 v[18:33], v[110:113], v[66:69], v[18:33]
	s_waitcnt lgkmcnt(1)
	v_mfma_f32_32x32x16_bf16 v[34:49], v[98:101], v[66:69], v[34:49]
	ds_read_b128 v[66:69], v212 offset:22528
	v_mfma_f32_32x32x16_bf16 v[50:65], v[98:101], v[90:93], v[50:65]
	s_waitcnt lgkmcnt(1)
	v_mfma_f32_32x32x16_bf16 v[2:17], v[70:73], v[94:97], v[2:17]
	v_mfma_f32_32x32x16_bf16 v[18:33], v[70:73], v[74:77], v[18:33]
	ds_read_b128 v[78:81], v212 offset:3072
	s_waitcnt lgkmcnt(1)
	v_mfma_f32_32x32x16_bf16 v[50:65], v[66:69], v[94:97], v[50:65]
	ds_read_b128 v[90:93], v174 offset:33056
	ds_read_b128 v[94:97], v174 offset:33088
	ds_read_b128 v[98:101], v174 offset:33120
	ds_read_b128 v[70:73], v174 offset:33152
	v_mfma_f32_32x32x16_bf16 v[34:49], v[66:69], v[74:77], v[34:49]
	ds_read_b128 v[66:69], v212 offset:4096
	ds_read_b128 v[74:77], v212 offset:5120
	s_waitcnt lgkmcnt(3)
	v_mfma_f32_32x32x16_bf16 v[102:117], v[78:81], v[126:129], v[86:101]
	v_mfma_f32_32x32x16_bf16 v[86:101], v[78:81], v[134:137], v[86:101]
	s_waitcnt lgkmcnt(1)
	v_mfma_f32_32x32x16_bf16 v[86:101], v[66:69], v[146:149], v[86:101]
	v_mfma_f32_32x32x16_bf16 v[102:117], v[66:69], v[122:125], v[102:117]
	ds_read_b128 v[66:69], v212 offset:6144
	s_waitcnt lgkmcnt(1)
	v_mfma_f32_32x32x16_bf16 v[86:101], v[74:77], v[142:145], v[86:101]
	v_mfma_f32_32x32x16_bf16 v[102:117], v[74:77], v[130:133], v[102:117]
	ds_read_b128 v[74:77], v212 offset:15360
	s_waitcnt lgkmcnt(1)
	v_mfma_f32_32x32x16_bf16 v[86:101], v[66:69], v[138:141], v[86:101]
	v_mfma_f32_32x32x16_bf16 v[102:117], v[66:69], v[118:121], v[102:117]
	s_nop 10
	v_cvt_pk_bf16_f32 v78, v86, v87
	v_cvt_pk_bf16_f32 v80, v90, v91
	v_cvt_pk_bf16_f32 v79, v88, v89
	v_cvt_pk_bf16_f32 v81, v92, v93
	ds_read_b128 v[86:89], v212 offset:16384
	ds_read_b128 v[90:93], v212 offset:23552
	v_cvt_pk_bf16_f32 v66, v102, v103
	v_cvt_pk_bf16_f32 v67, v104, v105
	v_cvt_pk_bf16_f32 v68, v106, v107
	v_cvt_pk_bf16_f32 v69, v108, v109
	v_pk_max_i16 v66, v66, 0
	v_pk_max_i16 v67, v67, 0
	v_pk_max_i16 v68, v68, 0
	v_pk_max_i16 v69, v69, 0
	v_pk_max_i16 v78, v78, 0
	v_pk_max_i16 v79, v79, 0
	v_pk_max_i16 v80, v80, 0
	v_pk_max_i16 v81, v81, 0
	v_cvt_pk_bf16_f32 v94, v94, v95
	s_waitcnt lgkmcnt(2)
	v_mfma_f32_32x32x16_bf16 v[18:33], v[74:77], v[78:81], v[18:33]
	v_cvt_pk_bf16_f32 v95, v96, v97
	v_cvt_pk_bf16_f32 v96, v98, v99
	v_cvt_pk_bf16_f32 v97, v100, v101
	v_pk_max_i16 v94, v94, 0
	v_pk_max_i16 v95, v95, 0
	v_pk_max_i16 v96, v96, 0
	v_pk_max_i16 v97, v97, 0
	v_mfma_f32_32x32x16_bf16 v[2:17], v[74:77], v[66:69], v[2:17]
	v_cvt_pk_bf16_f32 v74, v110, v111
	v_cvt_pk_bf16_f32 v75, v112, v113
	v_cvt_pk_bf16_f32 v76, v114, v115
	v_cvt_pk_bf16_f32 v77, v116, v117
	v_pk_max_i16 v74, v74, 0
	v_pk_max_i16 v75, v75, 0
	v_pk_max_i16 v76, v76, 0
	v_pk_max_i16 v77, v77, 0
	s_waitcnt lgkmcnt(0)
	v_mfma_f32_32x32x16_bf16 v[50:65], v[90:93], v[66:69], v[50:65]
	ds_read_b128 v[66:69], v212 offset:24576
	v_mfma_f32_32x32x16_bf16 v[34:49], v[90:93], v[78:81], v[34:49]
	ds_read_b128 v[102:105], v212 offset:7168
	v_mfma_f32_32x32x16_bf16 v[2:17], v[86:89], v[74:77], v[2:17]
	s_waitcnt lgkmcnt(1)
	v_mfma_f32_32x32x16_bf16 v[50:65], v[66:69], v[74:77], v[50:65]
	ds_read_b128 v[74:77], v174 offset:33184
	ds_read_b128 v[78:81], v174 offset:33216
	v_mfma_f32_32x32x16_bf16 v[34:49], v[66:69], v[94:97], v[34:49]
	ds_read_b128 v[66:69], v212 offset:8192
	v_mfma_f32_32x32x16_bf16 v[18:33], v[86:89], v[94:97], v[18:33]
	s_waitcnt lgkmcnt(1)
	v_mfma_f32_32x32x16_bf16 v[86:101], v[102:105], v[126:129], v[70:85]
	v_mfma_f32_32x32x16_bf16 v[70:85], v[102:105], v[134:137], v[70:85]
	ds_read_b128 v[102:105], v212 offset:9216
	v_lshlrev_b32_e32 v135, 2, v1
	v_add_u32_e32 v134, v172, v174
	s_waitcnt lgkmcnt(1)
	v_mfma_f32_32x32x16_bf16 v[86:101], v[66:69], v[122:125], v[86:101]
	v_mfma_f32_32x32x16_bf16 v[70:85], v[66:69], v[146:149], v[70:85]
	ds_read_b128 v[66:69], v212 offset:10240
	s_waitcnt lgkmcnt(1)
	v_mfma_f32_32x32x16_bf16 v[86:101], v[102:105], v[130:133], v[86:101]
	v_mfma_f32_32x32x16_bf16 v[70:85], v[102:105], v[142:145], v[70:85]
	ds_read_b128 v[102:105], v212 offset:17408
	s_waitcnt lgkmcnt(1)
	v_mfma_f32_32x32x16_bf16 v[86:101], v[66:69], v[118:121], v[86:101]
	v_mfma_f32_32x32x16_bf16 v[70:85], v[66:69], v[138:141], v[70:85]
	s_nop 10
	v_cvt_pk_bf16_f32 v68, v90, v91
	v_cvt_pk_bf16_f32 v69, v92, v93
	ds_read_b128 v[90:93], v212 offset:25600
	v_cvt_pk_bf16_f32 v66, v86, v87
	v_cvt_pk_bf16_f32 v67, v88, v89
	v_pk_max_i16 v66, v66, 0
	v_pk_max_i16 v67, v67, 0
	v_pk_max_i16 v68, v68, 0
	v_pk_max_i16 v69, v69, 0
	v_cvt_pk_bf16_f32 v70, v70, v71
	v_cvt_pk_bf16_f32 v71, v72, v73
	s_waitcnt lgkmcnt(1)
	v_mfma_f32_32x32x16_bf16 v[2:17], v[102:105], v[66:69], v[2:17]
	v_cvt_pk_bf16_f32 v72, v74, v75
	v_cvt_pk_bf16_f32 v73, v76, v77
	ds_read_b128 v[74:77], v212 offset:18432
	v_cvt_pk_bf16_f32 v86, v94, v95
	v_cvt_pk_bf16_f32 v87, v96, v97
	v_cvt_pk_bf16_f32 v88, v98, v99
	s_waitcnt lgkmcnt(1)
	v_mfma_f32_32x32x16_bf16 v[50:65], v[90:93], v[66:69], v[50:65]
	ds_read_b128 v[66:69], v212 offset:26624
	v_cvt_pk_bf16_f32 v89, v100, v101
	v_pk_max_i16 v86, v86, 0
	v_pk_max_i16 v87, v87, 0
	v_pk_max_i16 v88, v88, 0
	v_pk_max_i16 v89, v89, 0
	v_pk_max_i16 v70, v70, 0
	v_pk_max_i16 v71, v71, 0
	v_pk_max_i16 v72, v72, 0
	v_pk_max_i16 v73, v73, 0
	v_cvt_pk_bf16_f32 v78, v78, v79
	v_cvt_pk_bf16_f32 v79, v80, v81
	s_waitcnt lgkmcnt(1)
	v_mfma_f32_32x32x16_bf16 v[2:17], v[74:77], v[86:89], v[2:17]
	v_cvt_pk_bf16_f32 v80, v82, v83
	v_cvt_pk_bf16_f32 v81, v84, v85
	v_pk_max_i16 v78, v78, 0
	v_pk_max_i16 v79, v79, 0
	v_pk_max_i16 v80, v80, 0
	v_pk_max_i16 v81, v81, 0
	s_waitcnt lgkmcnt(0)
	v_mfma_f32_32x32x16_bf16 v[50:65], v[66:69], v[86:89], v[50:65]
	v_mfma_f32_32x32x16_bf16 v[34:49], v[90:93], v[70:73], v[34:49]
	s_nop 10
	v_add_f32_e32 v130, v10, v58
	v_add_f32_e32 v131, v11, v59
	v_add_f32_e32 v132, v12, v60
	v_add_f32_e32 v133, v13, v61
	v_add_f32_e32 v138, v4, v52
	v_add_f32_e32 v139, v5, v53
	v_pk_add_f32 v[140:141], v[16:17], v[64:65]
	v_pk_add_f32 v[142:143], v[8:9], v[56:57]
	v_pk_add_f32 v[144:145], v[14:15], v[62:63]
	v_pk_add_f32 v[146:147], v[6:7], v[54:55]
	v_mfma_f32_32x32x16_bf16 v[18:33], v[102:105], v[70:73], v[18:33]
	ds_read2st64_b32 v[70:71], v135 offset0:133 offset1:134
	v_add_f32_e32 v148, v2, v50
	v_add_f32_e32 v149, v3, v51
	v_add_f32_e32 v144, v146, v144
	v_add_f32_e32 v145, v147, v145
	v_pk_add_f32 v[140:141], v[142:143], v[140:141]
	v_pk_add_f32 v[132:133], v[138:139], v[132:133]
	v_pk_add_f32 v[130:131], v[148:149], v[130:131]
	v_pk_add_f32 v[132:133], v[132:133], v[140:141]
	v_pk_add_f32 v[130:131], v[130:131], v[144:145]
	v_mfma_f32_32x32x16_bf16 v[34:49], v[66:69], v[78:81], v[34:49]
	v_pk_mov_b32 v[138:139], v[130:131], v[132:133] op_sel:[1,0]
	v_mov_b32_e32 v131, v133
	s_waitcnt vmcnt(0) lgkmcnt(0)
	v_mul_f32_e32 v66, v175, v70
	v_pk_add_f32 v[130:131], v[138:139], v[130:131]
	ds_write_b32 v173, v66 offset:512
	v_mul_f32_e32 v66, v175, v71
	v_pk_add_f32 v[130:131], v[130:131], v[130:131] op_sel:[0,1] op_sel_hi:[1,0]
	s_waitcnt lgkmcnt(0)
	ds_read_b128 v[102:105], v174 offset:34560
	ds_read_b128 v[98:101], v174 offset:34592
	ds_read_b128 v[110:113], v174 offset:34624
	ds_read_b128 v[106:109], v174 offset:34656
	ds_read_b128 v[114:117], v174 offset:34688
	ds_read_b128 v[122:125], v174 offset:34720
	ds_read_b128 v[118:121], v174 offset:34752
	ds_read_b128 v[126:129], v174 offset:34784
	v_mov_b32_dpp v66, v66 quad_perm:[1,0,3,2] row_mask:0xf bank_mask:0xf bound_ctrl:1
	v_mov_b32_e32 v131, v130
	v_fmac_f32_e32 v66, v175, v71
	s_nop 0
	v_permlane32_swap_b32_e32 v130, v131
	v_add_f32_dpp v66, v66, v66 quad_perm:[2,3,0,1] row_mask:0xf bank_mask:0xf bound_ctrl:1
	v_add_f32_e32 v130, v130, v131
	v_fmamk_f32 v65, v130, 0xbc800000, v65
	v_add_f32_dpp v66, v66, v66 row_half_mirror row_mask:0xf bank_mask:0xf bound_ctrl:1
	v_fmamk_f32 v64, v130, 0xbc800000, v64
	v_fmamk_f32 v63, v130, 0xbc800000, v63
	v_fmamk_f32 v62, v130, 0xbc800000, v62
	v_fmamk_f32 v61, v130, 0xbc800000, v61
	v_fmamk_f32 v60, v130, 0xbc800000, v60
	v_fmamk_f32 v59, v130, 0xbc800000, v59
	v_fmamk_f32 v58, v130, 0xbc800000, v58
	v_fmamk_f32 v57, v130, 0xbc800000, v57
	v_fmamk_f32 v56, v130, 0xbc800000, v56
	v_fmamk_f32 v55, v130, 0xbc800000, v55
	v_fmamk_f32 v54, v130, 0xbc800000, v54
	v_fmamk_f32 v53, v130, 0xbc800000, v53
	v_fmamk_f32 v52, v130, 0xbc800000, v52
	v_fmamk_f32 v51, v130, 0xbc800000, v51
	v_fmac_f32_e32 v50, 0xbc800000, v130
	v_add_f32_dpp v66, v66, v66 row_ror:8 row_mask:0xf bank_mask:0xf bound_ctrl:1
	v_fmamk_f32 v17, v130, 0xbc800000, v17
	v_fmamk_f32 v16, v130, 0xbc800000, v16
	v_fmamk_f32 v15, v130, 0xbc800000, v15
	v_fmamk_f32 v14, v130, 0xbc800000, v14
	v_fmamk_f32 v13, v130, 0xbc800000, v13
	v_fmamk_f32 v12, v130, 0xbc800000, v12
	v_fmamk_f32 v11, v130, 0xbc800000, v11
	v_fmamk_f32 v10, v130, 0xbc800000, v10
	v_fmamk_f32 v9, v130, 0xbc800000, v9
	v_fmamk_f32 v8, v130, 0xbc800000, v8
	v_fmamk_f32 v7, v130, 0xbc800000, v7
	v_fmamk_f32 v6, v130, 0xbc800000, v6
	v_fmamk_f32 v5, v130, 0xbc800000, v5
	v_fmamk_f32 v4, v130, 0xbc800000, v4
	v_fmamk_f32 v3, v130, 0xbc800000, v3
	v_fmac_f32_e32 v2, 0xbc800000, v130
	v_pk_mul_f32 v[130:131], v[54:55], v[54:55]
	v_pk_mul_f32 v[132:133], v[62:63], v[62:63]
	v_pk_mul_f32 v[138:139], v[50:51], v[50:51]
	v_pk_mul_f32 v[140:141], v[58:59], v[58:59]
	v_pk_mul_f32 v[142:143], v[56:57], v[56:57]
	v_pk_mul_f32 v[144:145], v[64:65], v[64:65]
	v_pk_mul_f32 v[146:147], v[52:53], v[52:53]
	v_pk_mul_f32 v[148:149], v[60:61], v[60:61]
	v_mov_b32_e32 v67, v66
	v_pk_fma_f32 v[148:149], v[12:13], v[12:13], v[148:149]
	v_pk_fma_f32 v[146:147], v[4:5], v[4:5], v[146:147]
	v_pk_fma_f32 v[144:145], v[16:17], v[16:17], v[144:145]
	v_pk_fma_f32 v[142:143], v[8:9], v[8:9], v[142:143]
	v_pk_fma_f32 v[140:141], v[10:11], v[10:11], v[140:141]
	v_pk_fma_f32 v[138:139], v[2:3], v[2:3], v[138:139]
	v_pk_fma_f32 v[132:133], v[14:15], v[14:15], v[132:133]
	v_pk_fma_f32 v[130:131], v[6:7], v[6:7], v[130:131]
	v_permlane16_swap_b32_e32 v66, v67
	v_pk_add_f32 v[130:131], v[130:131], v[132:133]
	v_pk_add_f32 v[132:133], v[138:139], v[140:141]
	v_pk_add_f32 v[138:139], v[142:143], v[144:145]
	v_pk_add_f32 v[140:141], v[146:147], v[148:149]
	v_mfma_f32_32x32x16_bf16 v[18:33], v[74:77], v[78:81], v[18:33]
	v_add_f32_e32 v136, v66, v67
	ds_read_b128 v[70:73], v134 offset:512
	ds_read_b128 v[66:69], v134 offset:544
	ds_read_b128 v[78:81], v134 offset:576
	ds_read_b128 v[74:77], v134 offset:608
	ds_read_b128 v[82:85], v134 offset:640
	ds_read_b128 v[90:93], v134 offset:672
	ds_read_b128 v[86:89], v134 offset:704
	ds_read_b128 v[94:97], v134 offset:736
	v_pk_add_f32 v[138:139], v[140:141], v[138:139]
	v_pk_add_f32 v[130:131], v[132:133], v[130:131]
	s_waitcnt lgkmcnt(8)
	v_pk_mul_f32 v[140:141], v[126:127], v[62:63]
	v_pk_mov_b32 v[132:133], v[130:131], v[138:139] op_sel:[1,0]
	v_mov_b32_e32 v131, v139
	v_pk_mul_f32 v[138:139], v[122:123], v[54:55]
	v_pk_mul_f32 v[142:143], v[114:115], v[50:51]
	v_pk_mul_f32 v[144:145], v[118:119], v[58:59]
	v_pk_mul_f32 v[146:147], v[124:125], v[56:57]
	v_pk_mul_f32 v[148:149], v[128:129], v[64:65]
	v_pk_mul_f32 v[154:155], v[116:117], v[52:53]
	v_pk_mul_f32 v[156:157], v[120:121], v[60:61]
	v_pk_fma_f32 v[154:155], v[104:105], v[4:5], v[154:155]
	v_pk_fma_f32 v[156:157], v[112:113], v[12:13], v[156:157]
	v_pk_fma_f32 v[148:149], v[108:109], v[16:17], v[148:149]
	v_pk_fma_f32 v[146:147], v[100:101], v[8:9], v[146:147]
	v_pk_fma_f32 v[144:145], v[110:111], v[10:11], v[144:145]
	v_pk_fma_f32 v[142:143], v[102:103], v[2:3], v[142:143]
	v_pk_fma_f32 v[140:141], v[106:107], v[14:15], v[140:141]
	v_pk_fma_f32 v[138:139], v[98:99], v[6:7], v[138:139]
	v_pk_add_f32 v[130:131], v[132:133], v[130:131]
	v_pk_add_f32 v[138:139], v[138:139], v[140:141]
	v_pk_add_f32 v[140:141], v[142:143], v[144:145]
	v_pk_add_f32 v[142:143], v[146:147], v[148:149]
	v_pk_add_f32 v[144:145], v[154:155], v[156:157]
	v_pk_add_f32 v[132:133], v[130:131], v[130:131] op_sel:[0,1] op_sel_hi:[1,0]
	v_pk_add_f32 v[142:143], v[144:145], v[142:143]
	v_pk_add_f32 v[138:139], v[140:141], v[138:139]
	v_add_f32_e32 v133, v142, v143
	v_add_f32_e32 v130, v138, v139
	s_waitcnt lgkmcnt(2)
	v_pk_mul_f32 v[138:139], v[90:91], v[54:55]
	s_waitcnt lgkmcnt(0)
	v_pk_mul_f32 v[140:141], v[94:95], v[62:63]
	v_pk_mul_f32 v[142:143], v[82:83], v[50:51]
	v_pk_mul_f32 v[144:145], v[86:87], v[58:59]
	v_pk_mul_f32 v[146:147], v[92:93], v[56:57]
	v_pk_mul_f32 v[148:149], v[96:97], v[64:65]
	v_pk_mul_f32 v[154:155], v[84:85], v[52:53]
	v_pk_mul_f32 v[156:157], v[88:89], v[60:61]
	v_add_f32_e32 v130, v130, v133
	v_pk_fma_f32 v[156:157], v[80:81], v[12:13], v[156:157]
	v_pk_fma_f32 v[154:155], v[72:73], v[4:5], v[154:155]
	v_pk_fma_f32 v[148:149], v[76:77], v[16:17], v[148:149]
	v_pk_fma_f32 v[146:147], v[68:69], v[8:9], v[146:147]
	v_pk_fma_f32 v[144:145], v[78:79], v[10:11], v[144:145]
	v_pk_fma_f32 v[142:143], v[70:71], v[2:3], v[142:143]
	v_pk_fma_f32 v[140:141], v[74:75], v[14:15], v[140:141]
	v_pk_fma_f32 v[138:139], v[66:67], v[6:7], v[138:139]
	v_mov_b32_e32 v133, v130
	v_pk_add_f32 v[138:139], v[138:139], v[140:141]
	v_pk_add_f32 v[140:141], v[142:143], v[144:145]
	v_pk_add_f32 v[142:143], v[146:147], v[148:149]
	v_pk_add_f32 v[144:145], v[154:155], v[156:157]
	v_permlane32_swap_b32_e32 v130, v133
	v_pk_add_f32 v[142:143], v[144:145], v[142:143]
	v_add_f32_e32 v160, v130, v133
	v_pk_add_f32 v[138:139], v[140:141], v[138:139]
	v_add_f32_e32 v133, v142, v143
	v_pk_add_f32 v[140:141], v[26:27], v[42:43]
	v_pk_add_f32 v[142:143], v[28:29], v[44:45]
	v_pk_add_f32 v[144:145], v[20:21], v[36:37]
	v_pk_add_f32 v[146:147], v[32:33], v[48:49]
	v_pk_add_f32 v[148:149], v[24:25], v[40:41]
	v_pk_add_f32 v[154:155], v[30:31], v[46:47]
	v_pk_add_f32 v[156:157], v[22:23], v[38:39]
	v_pk_add_f32 v[158:159], v[18:19], v[34:35]
	v_pk_add_f32 v[154:155], v[156:157], v[154:155]
	v_pk_add_f32 v[146:147], v[148:149], v[146:147]
	v_pk_add_f32 v[142:143], v[144:145], v[142:143]
	v_pk_add_f32 v[140:141], v[158:159], v[140:141]
	v_pk_add_f32 v[142:143], v[142:143], v[146:147]
	v_pk_add_f32 v[140:141], v[140:141], v[154:155]
	v_add_f32_e32 v130, v138, v139
	v_pk_mov_b32 v[144:145], v[140:141], v[142:143] op_sel:[1,0]
	v_mov_b32_e32 v141, v143
	v_pk_add_f32 v[140:141], v[144:145], v[140:141]
	v_add_f32_e32 v133, v130, v133
	v_pk_add_f32 v[140:141], v[140:141], v[140:141] op_sel:[0,1] op_sel_hi:[1,0]
	v_mov_b32_e32 v131, v132
	v_mov_b32_e32 v130, v140
	s_nop 1
	v_permlane32_swap_b32_e32 v140, v130
	v_add_f32_e32 v130, v140, v130
	v_fmamk_f32 v49, v130, 0xbc800000, v49
	v_fmamk_f32 v48, v130, 0xbc800000, v48
	v_fmamk_f32 v47, v130, 0xbc800000, v47
	v_fmamk_f32 v46, v130, 0xbc800000, v46
	v_fmamk_f32 v45, v130, 0xbc800000, v45
	v_fmamk_f32 v44, v130, 0xbc800000, v44
	v_fmamk_f32 v43, v130, 0xbc800000, v43
	v_fmamk_f32 v42, v130, 0xbc800000, v42
	v_fmamk_f32 v41, v130, 0xbc800000, v41
	v_fmamk_f32 v40, v130, 0xbc800000, v40
	v_fmamk_f32 v39, v130, 0xbc800000, v39
	v_fmamk_f32 v38, v130, 0xbc800000, v38
	v_fmamk_f32 v37, v130, 0xbc800000, v37
	v_fmamk_f32 v36, v130, 0xbc800000, v36
	v_fmamk_f32 v35, v130, 0xbc800000, v35
	v_fmac_f32_e32 v34, 0xbc800000, v130
	v_fmamk_f32 v33, v130, 0xbc800000, v33
	v_fmamk_f32 v32, v130, 0xbc800000, v32
	v_fmamk_f32 v31, v130, 0xbc800000, v31
	v_fmamk_f32 v30, v130, 0xbc800000, v30
	v_fmamk_f32 v29, v130, 0xbc800000, v29
	v_fmamk_f32 v28, v130, 0xbc800000, v28
	v_fmamk_f32 v27, v130, 0xbc800000, v27
	v_fmamk_f32 v26, v130, 0xbc800000, v26
	v_fmamk_f32 v25, v130, 0xbc800000, v25
	v_fmamk_f32 v24, v130, 0xbc800000, v24
	v_fmamk_f32 v23, v130, 0xbc800000, v23
	v_fmamk_f32 v22, v130, 0xbc800000, v22
	v_fmamk_f32 v21, v130, 0xbc800000, v21
	v_fmamk_f32 v20, v130, 0xbc800000, v20
	v_fmamk_f32 v19, v130, 0xbc800000, v19
	v_fmac_f32_e32 v18, 0xbc800000, v130
	v_pk_mul_f32 v[140:141], v[38:39], v[38:39]
	v_pk_mul_f32 v[142:143], v[46:47], v[46:47]
	v_pk_mul_f32 v[144:145], v[34:35], v[34:35]
	v_pk_mul_f32 v[146:147], v[42:43], v[42:43]
	v_pk_mul_f32 v[148:149], v[40:41], v[40:41]
	v_pk_mul_f32 v[154:155], v[48:49], v[48:49]
	v_pk_mul_f32 v[156:157], v[36:37], v[36:37]
	v_pk_mul_f32 v[158:159], v[44:45], v[44:45]
	v_pk_fma_f32 v[156:157], v[20:21], v[20:21], v[156:157]
	v_pk_fma_f32 v[158:159], v[28:29], v[28:29], v[158:159]
	v_pk_fma_f32 v[154:155], v[32:33], v[32:33], v[154:155]
	v_pk_fma_f32 v[148:149], v[24:25], v[24:25], v[148:149]
	v_pk_fma_f32 v[146:147], v[26:27], v[26:27], v[146:147]
	v_pk_fma_f32 v[144:145], v[18:19], v[18:19], v[144:145]
	v_pk_fma_f32 v[142:143], v[30:31], v[30:31], v[142:143]
	v_pk_fma_f32 v[140:141], v[22:23], v[22:23], v[140:141]
	v_permlane32_swap_b32_e32 v132, v131
	v_pk_add_f32 v[140:141], v[140:141], v[142:143]
	v_pk_add_f32 v[142:143], v[144:145], v[146:147]
	v_pk_add_f32 v[144:145], v[148:149], v[154:155]
	v_pk_add_f32 v[146:147], v[156:157], v[158:159]
	v_pk_add_f32 v[140:141], v[142:143], v[140:141]
	v_pk_add_f32 v[144:145], v[146:147], v[144:145]
	v_pk_mul_f32 v[122:123], v[122:123], v[38:39]
	v_pk_mov_b32 v[142:143], v[140:141], v[144:145] op_sel:[1,0]
	v_mov_b32_e32 v141, v145
	v_pk_add_f32 v[140:141], v[142:143], v[140:141]
	v_pk_mul_f32 v[126:127], v[126:127], v[46:47]
	v_pk_add_f32 v[140:141], v[140:141], v[140:141] op_sel:[0,1] op_sel_hi:[1,0]
	v_pk_mul_f32 v[114:115], v[114:115], v[34:35]
	v_mov_b32_e32 v130, v140
	s_nop 1
	v_permlane32_swap_b32_e32 v140, v130
	v_mov_b32_e32 v141, v132
	v_pk_add_f32 v[130:131], v[140:141], v[130:131]
	v_pk_mul_f32 v[118:119], v[118:119], v[42:43]
	v_pk_fma_f32 v[130:131], v[130:131], s[0:1], v[152:153] op_sel_hi:[1,0,0]
	v_pk_mul_f32 v[124:125], v[124:125], v[40:41]
	v_mul_f32_e32 v132, 0x4b800000, v131
	v_cmp_gt_f32_e32 vcc, s1, v131
	v_pk_mul_f32 v[128:129], v[128:129], v[48:49]
	v_pk_mul_f32 v[116:117], v[116:117], v[36:37]
	v_pk_mul_f32 v[120:121], v[120:121], v[44:45]
	v_cndmask_b32_e32 v131, v131, v132, vcc
	v_mul_f32_e32 v132, 0x4b800000, v130
	v_cmp_gt_f32_e64 s[0:1], s1, v130
	v_pk_fma_f32 v[112:113], v[112:113], v[28:29], v[120:121]
	v_pk_fma_f32 v[104:105], v[104:105], v[20:21], v[116:117]
	v_pk_fma_f32 v[108:109], v[108:109], v[32:33], v[128:129]
	v_pk_fma_f32 v[100:101], v[100:101], v[24:25], v[124:125]
	v_pk_fma_f32 v[110:111], v[110:111], v[26:27], v[118:119]
	v_pk_fma_f32 v[102:103], v[102:103], v[18:19], v[114:115]
	v_pk_fma_f32 v[106:107], v[106:107], v[30:31], v[126:127]
	v_pk_fma_f32 v[98:99], v[98:99], v[22:23], v[122:123]
	v_rsq_f32_e32 v131, v131
	v_cndmask_b32_e64 v130, v130, v132, s[0:1]
	v_pk_add_f32 v[98:99], v[98:99], v[106:107]
	v_pk_add_f32 v[102:103], v[102:103], v[110:111]
	v_pk_add_f32 v[100:101], v[100:101], v[108:109]
	v_pk_add_f32 v[104:105], v[104:105], v[112:113]
	v_rsq_f32_e32 v132, v130
	v_pk_add_f32 v[100:101], v[104:105], v[100:101]
	v_pk_add_f32 v[98:99], v[102:103], v[98:99]
	v_mul_f32_e32 v130, 0x45800000, v131
	v_add_f32_e32 v98, v98, v99
	v_add_f32_e32 v99, v100, v101
	v_add_f32_e32 v98, v98, v99
	v_mov_b32_e32 v99, v98
	v_pk_mul_f32 v[90:91], v[90:91], v[38:39]
	v_pk_mul_f32 v[94:95], v[94:95], v[46:47]
	v_pk_mul_f32 v[82:83], v[82:83], v[34:35]
	v_pk_mul_f32 v[86:87], v[86:87], v[42:43]
	v_cndmask_b32_e32 v130, v131, v130, vcc
	v_mul_f32_e32 v131, 0x45800000, v132
	v_permlane32_swap_b32_e32 v98, v99
	v_pk_fma_f32 v[78:79], v[78:79], v[26:27], v[86:87]
	v_pk_fma_f32 v[70:71], v[70:71], v[18:19], v[82:83]
	v_pk_fma_f32 v[74:75], v[74:75], v[30:31], v[94:95]
	v_pk_fma_f32 v[66:67], v[66:67], v[22:23], v[90:91]
	v_cndmask_b32_e64 v131, v132, v131, s[0:1]
	v_add_f32_e32 v98, v98, v99
	v_pk_add_f32 v[66:67], v[66:67], v[74:75]
	v_pk_add_f32 v[70:71], v[70:71], v[78:79]
	v_mul_f32_e32 v139, v160, v130
	v_mul_f32_e32 v98, v98, v131
	v_pk_add_f32 v[66:67], v[70:71], v[66:67]
	v_cmp_gt_u32_e32 vcc, 32, v1
	v_add_f32_e32 v66, v66, v67
	v_pk_mul_f32 v[92:93], v[92:93], v[40:41]
	v_cndmask_b32_e32 v67, v98, v139, vcc
	v_add_f32_e32 v67, s12, v67
	v_pk_mul_f32 v[96:97], v[96:97], v[48:49]
	v_pk_mul_f32 v[84:85], v[84:85], v[36:37]
	v_pk_mul_f32 v[88:89], v[88:89], v[44:45]
	v_mul_f32_e32 v67, 0xbfb8aa3b, v67
	v_pk_fma_f32 v[80:81], v[80:81], v[28:29], v[88:89]
	v_pk_fma_f32 v[72:73], v[72:73], v[20:21], v[84:85]
	v_pk_fma_f32 v[76:77], v[76:77], v[32:33], v[96:97]
	v_pk_fma_f32 v[68:69], v[68:69], v[24:25], v[92:93]
	v_exp_f32_e32 v70, v67
	v_pk_add_f32 v[68:69], v[68:69], v[76:77]
	v_pk_add_f32 v[72:73], v[72:73], v[80:81]
	v_cmp_lt_i32_e64 s[0:1], 0, v151
	v_pk_add_f32 v[68:69], v[72:73], v[68:69]
	v_mov_b32_e32 v137, v136
	v_add_f32_e32 v67, v68, v69
	v_add_f32_e32 v67, v66, v67
	v_add_f32_e32 v66, 1.0, v70
	v_rcp_f32_e32 v66, v66
	v_mov_b32_e32 v69, 0xff800000
	v_mov_b32_e32 v138, v133
	v_mov_b32_e32 v68, v67
	v_cndmask_b32_e64 v70, v69, v66, s[0:1]
	v_mbcnt_lo_u32_b32 v66, -1, 0
	v_mbcnt_hi_u32_b32 v66, -1, v66
	v_permlane32_swap_b32_e32 v136, v137
	v_permlane32_swap_b32_e32 v133, v138
	v_permlane32_swap_b32_e32 v67, v68
	v_and_b32_e32 v86, 64, v66
	s_mov_b32 s14, 8
	s_mov_b32 s13, 0
	v_mov_b32_e32 v66, 0
	s_waitcnt lgkmcnt(0)
